# gate-table loads batched (8 loads in flight per thread) on top of P0 GEMV pipelining and mLSTM LDS batching
# baseline (speedup 1.0000x reference)
.LBB0_126:
	v_ashrrev_i32_e32 v4, 2, v7
	v_and_b32_e32 v12, 12, v6
	v_mad_i64_i32 v[8:9], s[12:13], v4, s8, v[2:3]
	v_lshlrev_b32_e32 v4, 2, v12
	v_lshl_add_u64 v[8:9], v[8:9], 0, v[4:5]
	s_mov_b64 s[100:101], 0x302000
	global_load_dwordx4 v[20:23], v[8:9], off
	v_lshl_add_u64 v[8:9], v[8:9], 0, s[100:101]
	global_load_dwordx4 v[24:27], v[8:9], off
	v_lshl_add_u64 v[8:9], v[8:9], 0, s[100:101]
	global_load_dwordx4 v[28:31], v[8:9], off
	v_lshl_add_u64 v[8:9], v[8:9], 0, s[100:101]
	global_load_dwordx4 v[32:35], v[8:9], off
	v_lshl_add_u64 v[8:9], v[8:9], 0, s[100:101]
	global_load_dwordx4 v[36:39], v[8:9], off
	v_lshl_add_u64 v[8:9], v[8:9], 0, s[100:101]
	global_load_dwordx4 v[40:43], v[8:9], off
	v_lshl_add_u64 v[8:9], v[8:9], 0, s[100:101]
	global_load_dwordx4 v[44:47], v[8:9], off
	v_lshl_add_u64 v[8:9], v[8:9], 0, s[100:101]
	global_load_dwordx4 v[48:51], v[8:9], off
	v_and_b32_e32 v4, -4, v7
	v_lshlrev_b32_e32 v12, 12, v12
	v_add3_u32 v4, s9, v12, v4
	s_waitcnt vmcnt(7)
	ds_write2st64_b32 v4, v20, v21 offset1:16
	ds_write2st64_b32 v4, v22, v23 offset0:32 offset1:48
	v_add_u32_e32 v4, 0x200, v4
	s_waitcnt vmcnt(6)
	ds_write2st64_b32 v4, v24, v25 offset1:16
	ds_write2st64_b32 v4, v26, v27 offset0:32 offset1:48
	v_add_u32_e32 v4, 0x200, v4
	s_waitcnt vmcnt(5)
	ds_write2st64_b32 v4, v28, v29 offset1:16
	ds_write2st64_b32 v4, v30, v31 offset0:32 offset1:48
	v_add_u32_e32 v4, 0x200, v4
	s_waitcnt vmcnt(4)
	ds_write2st64_b32 v4, v32, v33 offset1:16
	ds_write2st64_b32 v4, v34, v35 offset0:32 offset1:48
	v_add_u32_e32 v4, 0x200, v4
	s_waitcnt vmcnt(3)
	ds_write2st64_b32 v4, v36, v37 offset1:16
	ds_write2st64_b32 v4, v38, v39 offset0:32 offset1:48
	v_add_u32_e32 v4, 0x200, v4
	s_waitcnt vmcnt(2)
	ds_write2st64_b32 v4, v40, v41 offset1:16
	ds_write2st64_b32 v4, v42, v43 offset0:32 offset1:48
	v_add_u32_e32 v4, 0x200, v4
	s_waitcnt vmcnt(1)
	ds_write2st64_b32 v4, v44, v45 offset1:16
	ds_write2st64_b32 v4, v46, v47 offset0:32 offset1:48
	v_add_u32_e32 v4, 0x200, v4
	s_waitcnt vmcnt(0)
	ds_write2st64_b32 v4, v48, v49 offset1:16
	ds_write2st64_b32 v4, v50, v51 offset0:32 offset1:48

.LBB0_1484:
	v_ashrrev_i32_e32 v4, 2, v7
	v_and_b32_e32 v12, 12, v6
	v_mad_i64_i32 v[8:9], s[8:9], v4, s5, v[2:3]
	v_lshlrev_b32_e32 v4, 2, v12
	v_lshl_add_u64 v[8:9], v[8:9], 0, v[4:5]
	s_mov_b64 s[100:101], 0x302000
	global_load_dwordx4 v[20:23], v[8:9], off
	v_lshl_add_u64 v[8:9], v[8:9], 0, s[100:101]
	global_load_dwordx4 v[24:27], v[8:9], off
	v_lshl_add_u64 v[8:9], v[8:9], 0, s[100:101]
	global_load_dwordx4 v[28:31], v[8:9], off
	v_lshl_add_u64 v[8:9], v[8:9], 0, s[100:101]
	global_load_dwordx4 v[32:35], v[8:9], off
	v_lshl_add_u64 v[8:9], v[8:9], 0, s[100:101]
	global_load_dwordx4 v[36:39], v[8:9], off
	v_lshl_add_u64 v[8:9], v[8:9], 0, s[100:101]
	global_load_dwordx4 v[40:43], v[8:9], off
	v_lshl_add_u64 v[8:9], v[8:9], 0, s[100:101]
	global_load_dwordx4 v[44:47], v[8:9], off
	v_lshl_add_u64 v[8:9], v[8:9], 0, s[100:101]
	global_load_dwordx4 v[48:51], v[8:9], off
	v_and_b32_e32 v4, -4, v7
	v_lshlrev_b32_e32 v12, 12, v12
	v_add3_u32 v4, s6, v12, v4
	s_waitcnt vmcnt(7)
	ds_write2st64_b32 v4, v20, v21 offset1:16
	ds_write2st64_b32 v4, v22, v23 offset0:32 offset1:48
	v_add_u32_e32 v4, 0x200, v4
	s_waitcnt vmcnt(6)
	ds_write2st64_b32 v4, v24, v25 offset1:16
	ds_write2st64_b32 v4, v26, v27 offset0:32 offset1:48
	v_add_u32_e32 v4, 0x200, v4
	s_waitcnt vmcnt(5)
	ds_write2st64_b32 v4, v28, v29 offset1:16
	ds_write2st64_b32 v4, v30, v31 offset0:32 offset1:48
	v_add_u32_e32 v4, 0x200, v4
	s_waitcnt vmcnt(4)
	ds_write2st64_b32 v4, v32, v33 offset1:16
	ds_write2st64_b32 v4, v34, v35 offset0:32 offset1:48
	v_add_u32_e32 v4, 0x200, v4
	s_waitcnt vmcnt(3)
	ds_write2st64_b32 v4, v36, v37 offset1:16
	ds_write2st64_b32 v4, v38, v39 offset0:32 offset1:48
	v_add_u32_e32 v4, 0x200, v4
	s_waitcnt vmcnt(2)
	ds_write2st64_b32 v4, v40, v41 offset1:16
	ds_write2st64_b32 v4, v42, v43 offset0:32 offset1:48
	v_add_u32_e32 v4, 0x200, v4
	s_waitcnt vmcnt(1)
	ds_write2st64_b32 v4, v44, v45 offset1:16
	ds_write2st64_b32 v4, v46, v47 offset0:32 offset1:48
	v_add_u32_e32 v4, 0x200, v4
	s_waitcnt vmcnt(0)
	ds_write2st64_b32 v4, v48, v49 offset1:16
	ds_write2st64_b32 v4, v50, v51 offset0:32 offset1:48
